# speedup vs baseline: 1.0027x; 1.0027x over previous
_ZN12_GLOBAL__N_113search_kernelEPKfS1_PhPf:
	s_load_dwordx2 s[8:9], s[0:1], 0x0
	s_load_dwordx2 s[4:5], s[0:1], 0x10
	s_movk_i32 s3, 0x90
	v_readfirstlane_b32 s10, v0
	v_cmp_gt_u32_e32 vcc, s3, v0
	s_and_saveexec_b64 s[6:7], vcc
	v_mov_b32_e32 v2, -1
	v_lshlrev_b32_e32 v1, 3, v0
	v_mov_b32_e32 v3, v2
	ds_write_b64 v1, v[2:3] offset:16384
	s_or_b64 exec, exec, s[6:7]
	s_waitcnt lgkmcnt(0)
	s_add_u32 s6, s4, 0x240000
	s_addc_u32 s7, s5, 0
	s_lshl_b32 s11, s2, 1
	s_and_b32 s14, s11, 14
	s_ashr_i32 s11, s2, 7
	s_lshr_b32 s15, s10, 6
	s_add_i32 s14, s14, s11
	s_bfe_u32 s2, s2, 0x40003
	s_mul_i32 s11, s15, 24
	v_mul_u32_u24_e32 v2, 0x71d, v0
	v_mul_u32_u24_e32 v4, 0x195, v0
	s_min_u32 s18, s11, 0xa5
	s_mul_i32 s11, s14, 3
	s_mul_i32 s12, s2, 9
	s_mov_b32 s13, 0
	v_lshrrev_b32_e32 v3, 16, v2
	s_movk_i32 s19, 0xffdc
	v_lshrrev_b32_e32 v5, 17, v4
	v_mad_i32_i24 v2, v3, s19, v0
	v_mad_i32_i24 v4, v5, -9, v3
	v_add_u32_e32 v3, s11, v5
	v_mov_b64_e32 v[6:7], s[12:13]
	v_mad_i64_i32 v[8:9], s[16:17], v3, s3, v[6:7]
	v_ashrrev_i32_e32 v5, 31, v4
	v_lshl_add_u64 v[4:5], v[8:9], 0, v[4:5]
	s_movk_i32 s13, 0x240
	v_mov_b64_e32 v[8:9], s[8:9]
	v_mad_u64_u32 v[10:11], s[8:9], v4, s13, v[8:9]
	v_min_u32_e32 v4, 0x1cb, v0
	v_or_b32_e32 v4, 0x200, v4
	v_mad_i32_i24 v11, v5, s13, v11
	v_mul_u32_u24_e32 v5, 0x71d, v4
	v_ashrrev_i32_e32 v3, 31, v2
	v_lshrrev_b32_e32 v5, 16, v5
	v_lshl_add_u64 v[2:3], v[2:3], 4, v[10:11]
	v_mad_i32_i24 v10, v5, s19, v4
	v_mul_u32_u24_e32 v4, 0x653, v4
	v_lshrrev_b32_e32 v11, 19, v4
	v_mad_i32_i24 v4, v11, -9, v5
	v_add_u32_e32 v5, s11, v11
	v_mad_i64_i32 v[6:7], s[8:9], v5, s3, v[6:7]
	v_ashrrev_i32_e32 v5, 31, v4
	v_lshl_add_u64 v[4:5], v[6:7], 0, v[4:5]
	v_mad_u64_u32 v[12:13], s[8:9], v4, s13, v[8:9]
	s_mul_i32 s8, s14, 0x90
	s_barrier
	global_load_dwordx4 v[6:9], v[2:3], off
	s_add_i32 s3, s8, s12
	v_and_b32_e32 v210, 15, v0
	v_lshlrev_b32_e32 v252, 3, v210
	v_bfe_u32 v253, v0, 4, 2
	s_lshl_b32 s11, s3, 6
	v_and_b32_e32 v2, 48, v0
	s_mul_i32 s9, s14, 0xbd
	v_or3_b32 v2, s11, v2, v210
	s_add_i32 s18, s18, s9
	v_and_b32_e32 v1, 63, v0
	v_ashrrev_i32_e32 v3, 31, v2
	s_lshl_b32 s3, s18, 6
	v_mad_i32_i24 v13, v5, s13, v13
	v_lshl_add_u64 v[14:15], v[2:3], 4, s[4:5]
	v_or_b32_e32 v2, s3, v1
	v_ashrrev_i32_e32 v11, 31, v10
	v_ashrrev_i32_e32 v3, 31, v2
	v_lshl_add_u64 v[10:11], v[10:11], 4, v[12:13]
	v_lshl_add_u64 v[16:17], v[2:3], 4, s[6:7]
	global_load_dwordx4 v[2:5], v[14:15], off
	global_load_dwordx4 v[58:61], v[16:17], off nt
	s_add_i32 s12, s3, 64
	global_load_dwordx4 v[10:13], v[10:11], off
	v_or_b32_e32 v14, s12, v1
	v_ashrrev_i32_e32 v15, 31, v14
	v_lshl_add_u64 v[14:15], v[14:15], 4, s[6:7]
	s_add_i32 s12, s3, 0x80
	global_load_dwordx4 v[54:57], v[14:15], off nt
	v_or_b32_e32 v14, s12, v1
	v_ashrrev_i32_e32 v15, 31, v14
	v_lshl_add_u64 v[14:15], v[14:15], 4, s[6:7]
	s_add_i32 s12, s3, 0xc0
	global_load_dwordx4 v[98:101], v[14:15], off nt
	v_or_b32_e32 v14, s12, v1
	v_ashrrev_i32_e32 v15, 31, v14
	v_lshl_add_u64 v[14:15], v[14:15], 4, s[6:7]
	s_add_i32 s12, s11, 64
	global_load_dwordx4 v[82:85], v[14:15], off nt
	v_or_b32_e32 v14, s12, v1
	v_ashrrev_i32_e32 v15, 31, v14
	v_lshl_add_u64 v[14:15], v[14:15], 4, s[4:5]
	s_add_i32 s12, s11, 0x80
	global_load_dwordx4 v[34:37], v[14:15], off
	v_or_b32_e32 v14, s12, v1
	s_add_i32 s12, s11, 0xc0
	v_or_b32_e32 v16, s12, v1
	s_add_i32 s12, s11, 0x100
	v_or_b32_e32 v18, s12, v1
	s_add_i32 s12, s11, 0x140
	v_ashrrev_i32_e32 v15, 31, v14
	v_ashrrev_i32_e32 v17, 31, v16
	v_or_b32_e32 v20, s12, v1
	v_lshl_add_u64 v[14:15], v[14:15], 4, s[4:5]
	v_lshl_add_u64 v[16:17], v[16:17], 4, s[4:5]
	v_ashrrev_i32_e32 v21, 31, v20
	s_add_i32 s12, s11, 0x180
	global_load_dwordx4 v[30:33], v[14:15], off
	global_load_dwordx4 v[26:29], v[16:17], off
	v_lshl_add_u64 v[14:15], v[20:21], 4, s[4:5]
	v_or_b32_e32 v20, s12, v1
	v_ashrrev_i32_e32 v21, 31, v20
	s_add_i32 s12, s11, 0x1c0
	v_lshl_add_u64 v[38:39], v[20:21], 4, s[4:5]
	v_or_b32_e32 v20, s12, v1
	v_ashrrev_i32_e32 v21, 31, v20
	s_addk_i32 s11, 0x200
	v_lshl_add_u64 v[40:41], v[20:21], 4, s[4:5]
	v_or_b32_e32 v20, s11, v1
	v_ashrrev_i32_e32 v21, 31, v20
	s_add_i32 s11, s3, 0x100
	v_lshl_add_u64 v[42:43], v[20:21], 4, s[4:5]
	v_or_b32_e32 v20, s11, v1
	s_add_i32 s11, s3, 0x140
	v_or_b32_e32 v16, s11, v1
	v_ashrrev_i32_e32 v17, 31, v16
	s_add_i32 s11, s3, 0x180
	v_lshl_add_u64 v[46:47], v[16:17], 4, s[6:7]
	v_or_b32_e32 v16, s11, v1
	v_ashrrev_i32_e32 v17, 31, v16
	s_add_i32 s11, s3, 0x1c0
	v_lshl_add_u64 v[48:49], v[16:17], 4, s[6:7]
	v_or_b32_e32 v16, s11, v1
	v_ashrrev_i32_e32 v17, 31, v16
	s_add_i32 s11, s3, 0x200
	v_lshl_add_u64 v[50:51], v[16:17], 4, s[6:7]
	v_or_b32_e32 v16, s11, v1
	v_ashrrev_i32_e32 v17, 31, v16
	s_add_i32 s11, s3, 0x240
	v_lshl_add_u64 v[52:53], v[16:17], 4, s[6:7]
	v_or_b32_e32 v16, s11, v1
	v_ashrrev_i32_e32 v17, 31, v16
	s_add_i32 s11, s3, 0x280
	v_ashrrev_i32_e32 v19, 31, v18
	v_ashrrev_i32_e32 v21, 31, v20
	v_lshl_add_u64 v[66:67], v[16:17], 4, s[6:7]
	v_or_b32_e32 v16, s11, v1
	v_lshl_add_u64 v[18:19], v[18:19], 4, s[4:5]
	v_lshl_add_u64 v[44:45], v[20:21], 4, s[6:7]
	v_ashrrev_i32_e32 v17, 31, v16
	s_add_i32 s11, s3, 0x2c0
	global_load_dwordx4 v[22:25], v[18:19], off
	v_lshl_add_u64 v[86:87], v[16:17], 4, s[6:7]
	v_or_b32_e32 v16, s11, v1
	s_add_i32 s11, s3, 0x300
	global_load_dwordx4 v[18:21], v[14:15], off
	global_load_dwordx4 v[62:65], v[44:45], off nt
	v_lshlrev_b32_e32 v14, 4, v0
	s_waitcnt vmcnt(12)
	ds_write_b128 v14, v[6:9]
	v_or_b32_e32 v6, s11, v1
	v_ashrrev_i32_e32 v7, 31, v6
	s_add_i32 s11, s3, 0x340
	v_lshl_add_u64 v[142:143], v[6:7], 4, s[6:7]
	v_or_b32_e32 v6, s11, v1
	v_ashrrev_i32_e32 v7, 31, v6
	s_add_i32 s11, s3, 0x380
	v_lshl_add_u64 v[146:147], v[6:7], 4, s[6:7]
	v_or_b32_e32 v6, s11, v1
	v_ashrrev_i32_e32 v17, 31, v16
	v_ashrrev_i32_e32 v7, 31, v6
	v_lshl_add_u64 v[88:89], v[16:17], 4, s[6:7]
	s_waitcnt vmcnt(9)
	ds_write_b128 v14, v[10:13] offset:8192
	global_load_dwordx4 v[14:17], v[38:39], off
	global_load_dwordx4 v[10:13], v[40:41], off
	v_lshl_add_u64 v[38:39], v[6:7], 4, s[6:7]
	global_load_dwordx4 v[6:9], v[42:43], off
	global_load_dwordx4 v[94:97], v[46:47], off nt
	global_load_dwordx4 v[78:81], v[48:49], off nt
	global_load_dwordx4 v[74:77], v[50:51], off nt
	global_load_dwordx4 v[70:73], v[52:53], off nt
	s_add_i32 s11, s3, 0x3c0
	v_or_b32_e32 v40, s11, v1
	v_ashrrev_i32_e32 v41, 31, v40
	s_cmpk_lt_u32 s10, 0x100
	s_cbranch_scc1 .Lstag_skip
	s_nop 15
	s_nop 15
	s_nop 7
.Lstag_skip:
	v_mfma_f32_16x16x32_f16 v[102:105], v[58:61], v[2:5], 0
	v_lshl_add_u64 v[40:41], v[40:41], 4, s[6:7]
	global_load_dwordx4 v[66:69], v[66:67], off nt
	s_nop 0
	global_load_dwordx4 v[90:93], v[86:87], off nt
	s_nop 0
	global_load_dwordx4 v[86:89], v[88:89], off nt
	s_nop 0
	global_load_dwordx4 v[50:53], v[142:143], off nt
	global_load_dwordx4 v[46:49], v[146:147], off nt
	global_load_dwordx4 v[42:45], v[38:39], off nt
	s_nop 0
	global_load_dwordx4 v[38:41], v[40:41], off nt
	s_waitcnt vmcnt(22)
	v_mfma_f32_16x16x32_f16 v[106:109], v[54:57], v[2:5], 0
	s_mov_b32 s11, 0x7f000000
	v_mov_b32_e32 v159, 0
	v_mov_b32_e32 v171, 0
	s_waitcnt vmcnt(21)
	v_mfma_f32_16x16x32_f16 v[110:113], v[98:101], v[2:5], 0
	v_mov_b32_e32 v173, 0
	v_mov_b32_e32 v197, 0
	v_mov_b32_e32 v195, 0
	s_waitcnt vmcnt(20)
	v_mfma_f32_16x16x32_f16 v[114:117], v[82:85], v[2:5], 0
	v_mov_b32_e32 v199, 0
	v_min_i32_e32 v102, v102, v103
	v_min_i32_e32 v103, v104, v105
	v_min_i32_e32 v104, v106, v107
	v_min_i32_e32 v105, v108, v109
	v_min_i32_e32 v154, v110, v111
	v_min3_i32 v102, v102, v103, v104
	v_min_i32_e32 v155, v112, v113
	v_min_i32_e32 v114, v114, v115
	v_min3_i32 v102, v102, v105, v154
	s_waitcnt vmcnt(19)
	v_mfma_f32_16x16x32_f16 v[118:121], v[58:61], v[34:37], 0
	v_min_i32_e32 v115, v116, v117
	v_min3_i32 v102, v102, v155, v114
	v_min3_i32 v158, v102, v115, s11
	v_mfma_f32_16x16x32_f16 v[122:125], v[54:57], v[34:37], 0
	v_mov_b32_e32 v204, 0
	s_add_i32 s12, s3, 0x400
	v_mov_b32_e32 v205, 0
	v_mfma_f32_16x16x32_f16 v[126:129], v[98:101], v[34:37], 0
	v_mov_b32_e32 v220, 0
	v_mfma_f32_16x16x32_f16 v[130:133], v[82:85], v[34:37], 0
	s_waitcnt vmcnt(18)
	v_mfma_f32_16x16x32_f16 v[134:137], v[58:61], v[30:33], 0
	v_mfma_f32_16x16x32_f16 v[138:141], v[54:57], v[30:33], 0
	v_mfma_f32_16x16x32_f16 v[142:145], v[98:101], v[30:33], 0
	v_mfma_f32_16x16x32_f16 v[146:149], v[82:85], v[30:33], 0
	s_nop 0
	v_min_i32_e32 v102, v118, v119
	v_min_i32_e32 v103, v120, v121
	v_min_i32_e32 v104, v122, v123
	v_min_i32_e32 v105, v124, v125
	v_min_i32_e32 v114, v126, v127
	v_min3_i32 v102, v102, v103, v104
	v_min_i32_e32 v115, v128, v129
	v_min_i32_e32 v116, v130, v131
	v_min3_i32 v102, v102, v105, v114
	v_min_i32_e32 v117, v132, v133
	v_min3_i32 v102, v102, v115, v116
	s_waitcnt vmcnt(17)
	v_mfma_f32_16x16x32_f16 v[150:153], v[58:61], v[26:29], 0
	v_min3_i32 v170, v102, v117, s11
	v_mfma_f32_16x16x32_f16 v[106:109], v[54:57], v[26:29], 0
	v_mfma_f32_16x16x32_f16 v[110:113], v[98:101], v[26:29], 0
	v_mfma_f32_16x16x32_f16 v[154:157], v[82:85], v[26:29], 0
	s_nop 0
	v_min_i32_e32 v114, v134, v135
	v_min_i32_e32 v115, v136, v137
	v_min_i32_e32 v116, v138, v139
	v_min_i32_e32 v117, v140, v141
	v_min_i32_e32 v122, v142, v143
	v_min3_i32 v114, v114, v115, v116
	v_min_i32_e32 v123, v144, v145
	v_min_i32_e32 v124, v146, v147
	v_min3_i32 v114, v114, v117, v122
	v_min_i32_e32 v125, v148, v149
	v_min3_i32 v114, v114, v123, v124
	s_waitcnt vmcnt(16)
	v_mfma_f32_16x16x32_f16 v[160:163], v[58:61], v[22:25], 0
	v_min3_i32 v172, v114, v125, s11
	v_mfma_f32_16x16x32_f16 v[164:167], v[54:57], v[22:25], 0
	v_mfma_f32_16x16x32_f16 v[118:121], v[98:101], v[22:25], 0
	v_mfma_f32_16x16x32_f16 v[128:131], v[82:85], v[22:25], 0
	s_nop 0
	v_min_i32_e32 v110, v110, v111
	s_waitcnt vmcnt(15)
	v_mfma_f32_16x16x32_f16 v[174:177], v[58:61], v[18:21], 0
	v_min_i32_e32 v111, v112, v113
	v_min_i32_e32 v112, v154, v155
	v_min_i32_e32 v113, v156, v157
	s_waitcnt vmcnt(13)
	v_mfma_f32_16x16x32_f16 v[102:105], v[58:61], v[14:17], 0
	s_waitcnt vmcnt(12)
	v_mfma_f32_16x16x32_f16 v[134:137], v[58:61], v[10:13], 0
	s_waitcnt vmcnt(11)
	v_mfma_f32_16x16x32_f16 v[114:117], v[58:61], v[6:9], 0
	v_min_i32_e32 v58, v150, v151
	v_min_i32_e32 v59, v152, v153
	v_min_i32_e32 v60, v106, v107
	v_min_i32_e32 v61, v108, v109
	v_min3_i32 v58, v58, v59, v60
	v_min3_i32 v58, v58, v61, v110
	v_min3_i32 v58, v58, v111, v112
	v_mfma_f32_16x16x32_f16 v[178:181], v[54:57], v[18:21], 0
	v_min3_i32 v196, v58, v113, s11
	v_mfma_f32_16x16x32_f16 v[182:185], v[98:101], v[18:21], 0
	v_mfma_f32_16x16x32_f16 v[186:189], v[82:85], v[18:21], 0
	s_nop 0
	v_min_i32_e32 v110, v160, v161
	v_min_i32_e32 v111, v162, v163
	v_min_i32_e32 v112, v164, v165
	v_mfma_f32_16x16x32_f16 v[142:145], v[54:57], v[14:17], 0
	v_min_i32_e32 v113, v166, v167
	v_min_i32_e32 v118, v118, v119
	v_min_i32_e32 v119, v120, v121
	v_mfma_f32_16x16x32_f16 v[146:149], v[98:101], v[14:17], 0
	v_min_i32_e32 v120, v128, v129
	v_mfma_f32_16x16x32_f16 v[58:61], v[54:57], v[10:13], 0
	v_mfma_f32_16x16x32_f16 v[122:125], v[54:57], v[6:9], 0
	v_mfma_f32_16x16x32_f16 v[54:57], v[98:101], v[10:13], 0
	v_mfma_f32_16x16x32_f16 v[126:129], v[98:101], v[6:9], 0
	v_min3_i32 v99, v110, v111, v112
	v_min3_i32 v99, v99, v113, v118
	v_min_i32_e32 v98, v130, v131
	v_min3_i32 v99, v99, v119, v120
	v_mfma_f32_16x16x32_f16 v[106:109], v[82:85], v[14:17], 0
	v_min3_i32 v194, v99, v98, s11
	v_mfma_f32_16x16x32_f16 v[138:141], v[82:85], v[10:13], 0
	v_min_i32_e32 v98, v182, v183
	v_min_i32_e32 v99, v184, v185
	v_min_i32_e32 v100, v186, v187
	v_mfma_f32_16x16x32_f16 v[130:133], v[82:85], v[6:9], 0
	v_min_i32_e32 v82, v174, v175
	v_min_i32_e32 v83, v176, v177
	v_min_i32_e32 v84, v178, v179
	v_min_i32_e32 v85, v180, v181
	v_min3_i32 v82, v82, v83, v84
	v_min3_i32 v82, v82, v85, v98
	v_min_i32_e32 v101, v188, v189
	v_min3_i32 v82, v82, v99, v100
	v_min3_i32 v198, v82, v101, s11
	v_mfma_f32_16x16x32_f16 v[150:153], v[62:65], v[2:5], 0
	v_min_i32_e32 v82, v102, v103
	v_min_i32_e32 v83, v104, v105
	v_min_i32_e32 v84, v142, v143
	v_min_i32_e32 v85, v144, v145
	v_min_i32_e32 v98, v146, v147
	v_min3_i32 v82, v82, v83, v84
	v_min_i32_e32 v99, v148, v149
	v_min_i32_e32 v100, v106, v107
	v_min3_i32 v82, v82, v85, v98
	v_min_i32_e32 v101, v108, v109
	v_min3_i32 v82, v82, v99, v100
	v_min3_i32 v203, v82, v101, s11
	v_mfma_f32_16x16x32_f16 v[162:165], v[62:65], v[34:37], 0
	v_min_i32_e32 v58, v58, v59
	v_min_i32_e32 v59, v60, v61
	v_min_i32_e32 v54, v54, v55
	v_mfma_f32_16x16x32_f16 v[166:169], v[62:65], v[30:33], 0
	v_min_i32_e32 v55, v56, v57
	v_min_i32_e32 v56, v138, v139
	v_min_i32_e32 v57, v140, v141
	v_mfma_f32_16x16x32_f16 v[154:157], v[62:65], v[26:29], 0
	v_mfma_f32_16x16x32_f16 v[110:113], v[62:65], v[22:25], 0
	v_mfma_f32_16x16x32_f16 v[118:121], v[62:65], v[18:21], 0
	v_mfma_f32_16x16x32_f16 v[102:105], v[62:65], v[14:17], 0
	v_mfma_f32_16x16x32_f16 v[106:109], v[62:65], v[10:13], 0
	v_mfma_f32_16x16x32_f16 v[98:101], v[62:65], v[6:9], 0
	v_min_i32_e32 v62, v134, v135
	v_min_i32_e32 v63, v136, v137
	v_min3_i32 v58, v62, v63, v58
	v_min3_i32 v54, v58, v59, v54
	v_min3_i32 v54, v54, v55, v56
	v_min3_i32 v202, v54, v57, s11
	v_mov_b32_e32 v54, 0
	s_waitcnt vmcnt(10)
	v_mfma_f32_16x16x32_f16 v[174:177], v[94:97], v[2:5], 0
	v_add_u32_e32 v60, v1, v54
	v_add_u32_e32 v54, s12, v60
	s_add_i32 s12, s3, 0x440
	v_add_u32_e32 v56, s12, v60
	s_add_i32 s12, s3, 0x480
	v_add_u32_e32 v58, s12, v60
	s_add_i32 s12, s3, 0x4c0
	v_ashrrev_i32_e32 v55, 31, v54
	v_ashrrev_i32_e32 v57, 31, v56
	v_ashrrev_i32_e32 v59, 31, v58
	v_add_u32_e32 v60, s12, v60
	s_waitcnt vmcnt(9)
	v_mfma_f32_16x16x32_f16 v[134:137], v[78:81], v[2:5], 0
	v_lshl_add_u64 v[54:55], v[54:55], 4, s[6:7]
	v_lshl_add_u64 v[56:57], v[56:57], 4, s[6:7]
	v_lshl_add_u64 v[58:59], v[58:59], 4, s[6:7]
	s_waitcnt vmcnt(8)
	v_mfma_f32_16x16x32_f16 v[178:181], v[74:77], v[2:5], 0
	v_ashrrev_i32_e32 v61, 31, v60
	v_lshl_add_u64 v[138:139], v[60:61], 4, s[6:7]
	global_load_dwordx4 v[82:85], v[54:55], off nt
	global_load_dwordx4 v[62:65], v[56:57], off nt
	s_nop 0
	global_load_dwordx4 v[58:61], v[58:59], off nt
	s_nop 0
	global_load_dwordx4 v[54:57], v[138:139], off nt
	v_mfma_f32_16x16x32_f16 v[182:185], v[94:97], v[34:37], 0
	v_min_i32_e32 v114, v114, v115
	v_min_i32_e32 v115, v116, v117
	v_min_i32_e32 v116, v122, v123
	v_min_i32_e32 v117, v124, v125
	v_min_i32_e32 v122, v126, v127
	v_min3_i32 v114, v114, v115, v116
	v_min_i32_e32 v123, v128, v129
	v_min_i32_e32 v124, v130, v131
	v_min3_i32 v114, v114, v117, v122
	v_min_i32_e32 v125, v132, v133
	v_min3_i32 v114, v114, v123, v124
	v_mfma_f32_16x16x32_f16 v[206:209], v[78:81], v[34:37], 0
	v_min3_i32 v218, v114, v125, s11
	s_add_i32 s11, s3, 0x500
	s_mov_b32 s12, 0x2aaaaaab
	v_mfma_f32_16x16x32_f16 v[212:215], v[74:77], v[34:37], 0
	s_nop 0
	v_min3_i32 v114, v150, v151, v158
	v_min3_i32 v114, v152, v153, v114
	v_min3_i32 v114, v174, v175, v114
	v_min3_i32 v130, v176, v177, v114
	v_min3_i32 v130, v134, v135, v130
	v_min3_i32 v130, v136, v137, v130
	v_min3_i32 v130, v178, v179, v130
	v_min3_i32 v219, v180, v181, v130
	v_cmp_ge_i32_e32 vcc, v219, v158
	v_mfma_f32_16x16x32_f16 v[224:227], v[94:97], v[30:33], 0
	s_nop 0
	v_cndmask_b32_e32 v221, 1, v159, vcc
	v_mfma_f32_16x16x32_f16 v[228:231], v[78:81], v[30:33], 0
	v_mfma_f32_16x16x32_f16 v[232:235], v[74:77], v[30:33], 0
	s_nop 0
	v_min3_i32 v130, v162, v163, v170
	v_min3_i32 v130, v164, v165, v130
	v_min3_i32 v130, v182, v183, v130
	v_min3_i32 v130, v184, v185, v130
	v_min3_i32 v134, v206, v207, v130
	v_mfma_f32_16x16x32_f16 v[236:239], v[94:97], v[26:29], 0
	v_mfma_f32_16x16x32_f16 v[186:189], v[94:97], v[22:25], 0
	v_mfma_f32_16x16x32_f16 v[146:149], v[94:97], v[18:21], 0
	v_mfma_f32_16x16x32_f16 v[138:141], v[94:97], v[14:17], 0
	v_mfma_f32_16x16x32_f16 v[142:145], v[94:97], v[10:13], 0
	v_mfma_f32_16x16x32_f16 v[126:129], v[94:97], v[6:9], 0
	v_mfma_f32_16x16x32_f16 v[94:97], v[78:81], v[26:29], 0
	v_mfma_f32_16x16x32_f16 v[190:193], v[78:81], v[22:25], 0
	v_mfma_f32_16x16x32_f16 v[174:177], v[78:81], v[18:21], 0
	v_mfma_f32_16x16x32_f16 v[158:161], v[78:81], v[14:17], 0
	v_mfma_f32_16x16x32_f16 v[162:165], v[78:81], v[10:13], 0
	v_mfma_f32_16x16x32_f16 v[130:133], v[78:81], v[6:9], 0
	v_min3_i32 v78, v208, v209, v134
	v_min3_i32 v78, v212, v213, v78
	v_min3_i32 v217, v214, v215, v78
	v_cmp_ge_i32_e32 vcc, v217, v170
	v_mfma_f32_16x16x32_f16 v[122:125], v[74:77], v[26:29], 0
	s_nop 0
	v_cndmask_b32_e32 v222, 1, v171, vcc
	v_mfma_f32_16x16x32_f16 v[114:117], v[74:77], v[22:25], 0
	v_min3_i32 v78, v166, v167, v172
	v_min3_i32 v78, v168, v169, v78
	v_min3_i32 v78, v224, v225, v78
	v_min3_i32 v134, v226, v227, v78
	v_min3_i32 v134, v228, v229, v134
	v_min3_i32 v134, v230, v231, v134
	v_min3_i32 v134, v232, v233, v134
	v_min3_i32 v211, v234, v235, v134
	v_cmp_ge_i32_e32 vcc, v211, v172
	v_mfma_f32_16x16x32_f16 v[182:185], v[74:77], v[18:21], 0
	s_nop 0
	v_cndmask_b32_e32 v213, 1, v173, vcc
	v_mfma_f32_16x16x32_f16 v[178:181], v[74:77], v[14:17], 0
	v_mfma_f32_16x16x32_f16 v[78:81], v[74:77], v[10:13], 0
	v_mfma_f32_16x16x32_f16 v[150:153], v[74:77], v[6:9], 0
	v_min3_i32 v74, v154, v155, v196
	v_min3_i32 v74, v156, v157, v74
	v_min3_i32 v74, v236, v237, v74
	v_min3_i32 v74, v238, v239, v74
	v_min3_i32 v74, v94, v95, v74
	v_min3_i32 v74, v96, v97, v74
	v_min3_i32 v74, v122, v123, v74
	v_min3_i32 v212, v124, v125, v74
	v_cmp_ge_i32_e32 vcc, v212, v196
	s_waitcnt vmcnt(11)
	v_mfma_f32_16x16x32_f16 v[166:169], v[70:73], v[2:5], 0
	v_cndmask_b32_e32 v214, 1, v197, vcc
	v_mfma_f32_16x16x32_f16 v[170:173], v[70:73], v[34:37], 0
	v_min3_i32 v74, v110, v111, v194
	v_min3_i32 v74, v112, v113, v74
	v_min3_i32 v74, v186, v187, v74
	v_min3_i32 v74, v188, v189, v74
	v_min3_i32 v74, v190, v191, v74
	v_min3_i32 v74, v192, v193, v74
	v_min3_i32 v74, v114, v115, v74
	v_min3_i32 v215, v116, v117, v74
	v_cmp_ge_i32_e32 vcc, v215, v194
	v_mfma_f32_16x16x32_f16 v[154:157], v[70:73], v[30:33], 0
	s_nop 0
	v_cndmask_b32_e32 v216, 1, v195, vcc
	v_mfma_f32_16x16x32_f16 v[134:137], v[70:73], v[26:29], 0
	v_min3_i32 v74, v118, v119, v198
	v_min3_i32 v74, v120, v121, v74
	v_mfma_f32_16x16x32_f16 v[122:125], v[70:73], v[22:25], 0
	v_mfma_f32_16x16x32_f16 v[94:97], v[70:73], v[18:21], 0
	v_mfma_f32_16x16x32_f16 v[110:113], v[70:73], v[14:17], 0
	v_mfma_f32_16x16x32_f16 v[114:117], v[70:73], v[10:13], 0
	v_mfma_f32_16x16x32_f16 v[118:121], v[70:73], v[6:9], 0
	v_min3_i32 v70, v146, v147, v74
	v_min3_i32 v70, v148, v149, v70
	v_min3_i32 v70, v174, v175, v70
	v_min3_i32 v70, v176, v177, v70
	v_min3_i32 v70, v182, v183, v70
	v_min3_i32 v223, v184, v185, v70
	v_cmp_ge_i32_e32 vcc, v223, v198
	s_waitcnt vmcnt(10)
	v_mfma_f32_16x16x32_f16 v[186:189], v[66:69], v[2:5], 0
	v_cndmask_b32_e32 v244, 1, v199, vcc
	v_mfma_f32_16x16x32_f16 v[190:193], v[66:69], v[34:37], 0
	v_min3_i32 v70, v102, v103, v203
	v_min3_i32 v70, v104, v105, v70
	v_min3_i32 v70, v138, v139, v70
	v_min3_i32 v70, v140, v141, v70
	v_min3_i32 v70, v158, v159, v70
	v_min3_i32 v70, v160, v161, v70
	v_min3_i32 v70, v178, v179, v70
	v_min3_i32 v245, v180, v181, v70
	v_cmp_ge_i32_e32 vcc, v245, v203
	v_mfma_f32_16x16x32_f16 v[224:227], v[66:69], v[30:33], 0
	s_nop 0
	v_cndmask_b32_e32 v246, 1, v204, vcc
	v_mfma_f32_16x16x32_f16 v[198:201], v[66:69], v[26:29], 0
	v_min3_i32 v70, v106, v107, v202
	v_min3_i32 v70, v108, v109, v70
	v_min3_i32 v70, v142, v143, v70
	v_mfma_f32_16x16x32_f16 v[158:161], v[66:69], v[22:25], 0
	v_min3_i32 v70, v144, v145, v70
	v_min3_i32 v70, v162, v163, v70
	v_min3_i32 v70, v164, v165, v70
	v_mfma_f32_16x16x32_f16 v[146:149], v[66:69], v[18:21], 0
	v_min3_i32 v70, v78, v79, v70
	v_min3_i32 v247, v80, v81, v70
	v_cmp_ge_i32_e32 vcc, v247, v202
	v_mfma_f32_16x16x32_f16 v[138:141], v[66:69], v[14:17], 0
	s_nop 0
	v_cndmask_b32_e32 v248, 1, v205, vcc
	v_mfma_f32_16x16x32_f16 v[106:109], v[66:69], v[10:13], 0
	v_mfma_f32_16x16x32_f16 v[102:105], v[66:69], v[6:9], 0
	v_mov_b32_e32 v66, 0
	s_nop 0
	v_add_u32_e32 v72, v1, v66
	v_add_u32_e32 v66, s11, v72
	s_add_i32 s11, s3, 0x540
	v_add_u32_e32 v68, s11, v72
	s_add_i32 s11, s3, 0x580
	v_add_u32_e32 v70, s11, v72
	s_addk_i32 s3, 0x5c0
	v_ashrrev_i32_e32 v67, 31, v66
	v_ashrrev_i32_e32 v69, 31, v68
	v_ashrrev_i32_e32 v71, 31, v70
	v_add_u32_e32 v72, s3, v72
	s_waitcnt vmcnt(9)
	v_mfma_f32_16x16x32_f16 v[178:181], v[90:93], v[2:5], 0
	v_lshl_add_u64 v[66:67], v[66:67], 4, s[6:7]
	v_lshl_add_u64 v[68:69], v[68:69], 4, s[6:7]
	v_lshl_add_u64 v[70:71], v[70:71], 4, s[6:7]
	s_waitcnt vmcnt(8)
	v_mfma_f32_16x16x32_f16 v[194:197], v[86:89], v[2:5], 0
	v_ashrrev_i32_e32 v73, 31, v72
	v_lshl_add_u64 v[142:143], v[72:73], 4, s[6:7]
	global_load_dwordx4 v[78:81], v[66:67], off nt
	global_load_dwordx4 v[74:77], v[68:69], off nt
	s_nop 0
	global_load_dwordx4 v[70:73], v[70:71], off nt
	s_nop 0
	global_load_dwordx4 v[66:69], v[142:143], off nt
	v_mfma_f32_16x16x32_f16 v[228:231], v[90:93], v[34:37], 0
	v_min3_i32 v98, v98, v99, v218
	v_min3_i32 v98, v100, v101, v98
	v_min3_i32 v98, v126, v127, v98
	v_min3_i32 v98, v128, v129, v98
	v_min3_i32 v98, v130, v131, v98
	v_min3_i32 v98, v132, v133, v98
	v_min3_i32 v98, v150, v151, v98
	v_min3_i32 v249, v152, v153, v98
	v_cmp_ge_i32_e32 vcc, v249, v218
	v_mfma_f32_16x16x32_f16 v[232:235], v[86:89], v[34:37], 0
	s_mul_i32 s3, s15, 6
	v_cndmask_b32_e32 v218, 1, v220, vcc
	v_mfma_f32_16x16x32_f16 v[236:239], v[90:93], v[30:33], 0
	v_min3_i32 v98, v166, v167, v219
	s_mul_i32 s11, s2, 0x90
	v_mfma_f32_16x16x32_f16 v[206:209], v[90:93], v[26:29], 0
	v_mfma_f32_16x16x32_f16 v[182:185], v[90:93], v[22:25], 0
	v_mfma_f32_16x16x32_f16 v[174:177], v[90:93], v[18:21], 0
	v_mfma_f32_16x16x32_f16 v[162:165], v[90:93], v[14:17], 0
	v_mfma_f32_16x16x32_f16 v[142:145], v[90:93], v[10:13], 0
	v_mfma_f32_16x16x32_f16 v[126:129], v[90:93], v[6:9], 0
	v_min3_i32 v90, v168, v169, v98
	v_min3_i32 v90, v186, v187, v90
	v_min3_i32 v98, v188, v189, v90
	v_min3_i32 v98, v178, v179, v98
	v_min3_i32 v98, v180, v181, v98
	v_min3_i32 v98, v194, v195, v98
	v_min3_i32 v220, v196, v197, v98
	v_cmp_ge_i32_e32 vcc, v220, v219
	v_mfma_f32_16x16x32_f16 v[240:243], v[86:89], v[30:33], 0
	s_nop 0
	v_cndmask_b32_e32 v219, 2, v221, vcc
	v_mfma_f32_16x16x32_f16 v[90:93], v[86:89], v[26:29], 0
	v_min3_i32 v98, v170, v171, v217
	v_min3_i32 v98, v172, v173, v98
	v_min3_i32 v98, v190, v191, v98
	v_min3_i32 v98, v192, v193, v98
	v_min3_i32 v98, v228, v229, v98
	v_min3_i32 v98, v230, v231, v98
	v_min3_i32 v98, v232, v233, v98
	v_min3_i32 v221, v234, v235, v98
	v_cmp_ge_i32_e32 vcc, v221, v217
	v_mfma_f32_16x16x32_f16 v[202:205], v[86:89], v[22:25], 0
	s_nop 0
	v_cndmask_b32_e32 v217, 2, v222, vcc
	v_mfma_f32_16x16x32_f16 v[194:197], v[86:89], v[18:21], 0
	v_mfma_f32_16x16x32_f16 v[186:189], v[86:89], v[14:17], 0
	v_mfma_f32_16x16x32_f16 v[166:169], v[86:89], v[10:13], 0
	v_mfma_f32_16x16x32_f16 v[150:153], v[86:89], v[6:9], 0
	v_min3_i32 v86, v154, v155, v211
	v_min3_i32 v86, v156, v157, v86
	v_min3_i32 v86, v224, v225, v86
	v_min3_i32 v86, v226, v227, v86
	v_min3_i32 v86, v236, v237, v86
	v_min3_i32 v86, v238, v239, v86
	v_min3_i32 v86, v240, v241, v86
	v_min3_i32 v222, v242, v243, v86
	v_cmp_ge_i32_e32 vcc, v222, v211
	s_waitcnt vmcnt(11)
	v_mfma_f32_16x16x32_f16 v[170:173], v[50:53], v[2:5], 0
	v_cndmask_b32_e32 v211, 2, v213, vcc
	v_mfma_f32_16x16x32_f16 v[154:157], v[50:53], v[34:37], 0
	v_min3_i32 v86, v134, v135, v212
	v_min3_i32 v86, v136, v137, v86
	v_min3_i32 v86, v198, v199, v86
	v_min3_i32 v86, v200, v201, v86
	v_min3_i32 v86, v206, v207, v86
	v_min3_i32 v86, v208, v209, v86
	v_min3_i32 v86, v90, v91, v86
	v_min3_i32 v198, v92, v93, v86
	v_cmp_ge_i32_e32 vcc, v198, v212
	s_waitcnt vmcnt(10)
	v_mfma_f32_16x16x32_f16 v[134:137], v[46:49], v[2:5], 0
	v_cndmask_b32_e32 v199, 2, v214, vcc
	v_mfma_f32_16x16x32_f16 v[178:181], v[50:53], v[30:33], 0
	v_min3_i32 v122, v122, v123, v215
	v_min3_i32 v122, v124, v125, v122
	v_min3_i32 v122, v158, v159, v122
	v_min3_i32 v122, v160, v161, v122
	v_min3_i32 v122, v182, v183, v122
	v_min3_i32 v122, v184, v185, v122
	v_min3_i32 v122, v202, v203, v122
	v_min3_i32 v200, v204, v205, v122
	v_cmp_ge_i32_e32 vcc, v200, v215
	s_waitcnt vmcnt(9)
	v_mfma_f32_16x16x32_f16 v[158:161], v[42:45], v[2:5], 0
	v_cndmask_b32_e32 v201, 2, v216, vcc
	s_waitcnt vmcnt(8)
	v_mfma_f32_16x16x32_f16 v[182:185], v[38:41], v[2:5], 0
	v_min3_i32 v94, v94, v95, v223
	v_min3_i32 v94, v96, v97, v94
	v_min3_i32 v94, v146, v147, v94
	v_min3_i32 v94, v148, v149, v94
	v_min3_i32 v94, v174, v175, v94
	v_min3_i32 v94, v176, v177, v94
	v_min3_i32 v94, v194, v195, v94
	v_min3_i32 v202, v196, v197, v94
	v_cmp_ge_i32_e32 vcc, v202, v223
	v_mfma_f32_16x16x32_f16 v[146:149], v[46:49], v[34:37], 0
	s_nop 0
	v_cndmask_b32_e32 v203, 2, v244, vcc
	v_mfma_f32_16x16x32_f16 v[174:177], v[42:45], v[34:37], 0
	v_min3_i32 v94, v110, v111, v245
	v_min3_i32 v94, v112, v113, v94
	v_min3_i32 v94, v138, v139, v94
	v_min3_i32 v94, v140, v141, v94
	v_min3_i32 v94, v162, v163, v94
	v_min3_i32 v94, v164, v165, v94
	v_min3_i32 v94, v186, v187, v94
	v_min3_i32 v204, v188, v189, v94
	v_cmp_ge_i32_e32 vcc, v204, v245
	v_mfma_f32_16x16x32_f16 v[194:197], v[38:41], v[34:37], 0
	s_nop 0
	v_cndmask_b32_e32 v205, 2, v246, vcc
	v_mfma_f32_16x16x32_f16 v[110:113], v[46:49], v[30:33], 0
	v_min3_i32 v94, v114, v115, v247
	v_min3_i32 v94, v116, v117, v94
	v_min3_i32 v94, v106, v107, v94
	v_min3_i32 v94, v108, v109, v94
	v_min3_i32 v94, v142, v143, v94
	v_min3_i32 v94, v144, v145, v94
	v_min3_i32 v94, v166, v167, v94
	v_min3_i32 v206, v168, v169, v94
	v_cmp_ge_i32_e32 vcc, v206, v247
	v_mfma_f32_16x16x32_f16 v[190:193], v[50:53], v[26:29], 0
	s_nop 0
	v_cndmask_b32_e32 v207, 2, v248, vcc
	v_mfma_f32_16x16x32_f16 v[138:141], v[46:49], v[26:29], 0
	v_min3_i32 v114, v118, v119, v249
	v_min3_i32 v114, v120, v121, v114
	v_min3_i32 v102, v102, v103, v114
	v_min3_i32 v102, v104, v105, v102
	v_min3_i32 v102, v126, v127, v102
	v_min3_i32 v102, v128, v129, v102
	v_min3_i32 v102, v150, v151, v102
	v_min3_i32 v208, v152, v153, v102
	v_cmp_ge_i32_e32 vcc, v208, v249
	v_mfma_f32_16x16x32_f16 v[118:121], v[42:45], v[30:33], 0
	s_nop 0
	v_cndmask_b32_e32 v209, 2, v218, vcc
	v_mfma_f32_16x16x32_f16 v[126:129], v[38:41], v[30:33], 0
	v_min3_i32 v102, v170, v171, v220
	v_min3_i32 v102, v172, v173, v102
	v_min3_i32 v102, v134, v135, v102
	v_min3_i32 v102, v136, v137, v102
	v_min3_i32 v102, v158, v159, v102
	v_min3_i32 v102, v160, v161, v102
	v_min3_i32 v102, v182, v183, v102
	v_min3_i32 v182, v184, v185, v102
	v_cmp_ge_i32_e32 vcc, v182, v220
	v_mfma_f32_16x16x32_f16 v[142:145], v[42:45], v[26:29], 0
	s_nop 0
	v_cndmask_b32_e32 v183, 3, v219, vcc
	v_mfma_f32_16x16x32_f16 v[150:153], v[38:41], v[26:29], 0
	v_min3_i32 v102, v154, v155, v221
	v_min3_i32 v102, v156, v157, v102
	v_min3_i32 v102, v146, v147, v102
	v_min3_i32 v134, v148, v149, v102
	v_min3_i32 v134, v174, v175, v134
	v_min3_i32 v134, v176, v177, v134
	v_min3_i32 v134, v194, v195, v134
	v_min3_i32 v174, v196, v197, v134
	v_cmp_ge_i32_e32 vcc, v174, v221
	v_mfma_f32_16x16x32_f16 v[130:133], v[50:53], v[22:25], 0
	s_nop 0
	v_cndmask_b32_e32 v175, 3, v217, vcc
	v_mfma_f32_16x16x32_f16 v[186:189], v[46:49], v[22:25], 0
	v_min3_i32 v134, v178, v179, v222
	v_min3_i32 v134, v180, v181, v134
	v_min3_i32 v110, v110, v111, v134
	v_min3_i32 v110, v112, v113, v110
	v_min3_i32 v110, v118, v119, v110
	v_min3_i32 v110, v120, v121, v110
	v_min3_i32 v110, v126, v127, v110
	v_min3_i32 v176, v128, v129, v110
	v_cmp_ge_i32_e32 vcc, v176, v222
	v_mfma_f32_16x16x32_f16 v[166:169], v[42:45], v[22:25], 0
	s_nop 0
	v_cndmask_b32_e32 v177, 3, v211, vcc
	v_mfma_f32_16x16x32_f16 v[170:173], v[38:41], v[22:25], 0
	s_nop 0
	v_min3_i32 v118, v190, v191, v198
	v_mfma_f32_16x16x32_f16 v[162:165], v[38:41], v[18:21], 0
	v_mfma_f32_16x16x32_f16 v[146:149], v[38:41], v[14:17], 0
	v_mfma_f32_16x16x32_f16 v[126:129], v[38:41], v[10:13], 0
	v_mfma_f32_16x16x32_f16 v[110:113], v[38:41], v[6:9], 0
	v_min3_i32 v38, v192, v193, v118
	v_min3_i32 v38, v138, v139, v38
	v_min3_i32 v38, v140, v141, v38
	v_min3_i32 v38, v142, v143, v38
	v_min3_i32 v38, v144, v145, v38
	v_min3_i32 v38, v150, v151, v38
	v_min3_i32 v178, v152, v153, v38
	v_cmp_ge_i32_e32 vcc, v178, v198
	v_mfma_f32_16x16x32_f16 v[98:101], v[50:53], v[18:21], 0
	s_nop 0
	v_cndmask_b32_e32 v179, 3, v199, vcc
	v_mfma_f32_16x16x32_f16 v[122:125], v[46:49], v[18:21], 0
	v_mfma_f32_16x16x32_f16 v[158:161], v[42:45], v[18:21], 0
	s_nop 0
	v_min3_i32 v38, v130, v131, v200
	v_min3_i32 v38, v132, v133, v38
	v_min3_i32 v38, v186, v187, v38
	v_min3_i32 v38, v188, v189, v38
	v_min3_i32 v38, v166, v167, v38
	v_min3_i32 v38, v168, v169, v38
	v_min3_i32 v38, v170, v171, v38
	v_min3_i32 v166, v172, v173, v38
	v_cmp_ge_i32_e32 vcc, v166, v200
	v_mfma_f32_16x16x32_f16 v[86:89], v[50:53], v[14:17], 0
	s_nop 0
	v_cndmask_b32_e32 v167, 3, v201, vcc
	v_mfma_f32_16x16x32_f16 v[106:109], v[46:49], v[14:17], 0
	v_mfma_f32_16x16x32_f16 v[114:117], v[42:45], v[14:17], 0
	s_nop 0
	v_min3_i32 v38, v98, v99, v202
	v_min3_i32 v38, v100, v101, v38
	v_min3_i32 v38, v122, v123, v38
	v_min3_i32 v38, v124, v125, v38
	v_min3_i32 v38, v158, v159, v38
	v_min3_i32 v38, v160, v161, v38
	v_min3_i32 v122, v162, v163, v38
	v_min3_i32 v158, v164, v165, v122
	v_cmp_ge_i32_e32 vcc, v158, v202
	v_mfma_f32_16x16x32_f16 v[90:93], v[50:53], v[10:13], 0
	s_nop 0
	v_cndmask_b32_e32 v159, 3, v203, vcc
	v_mfma_f32_16x16x32_f16 v[94:97], v[46:49], v[10:13], 0
	v_mfma_f32_16x16x32_f16 v[102:105], v[42:45], v[10:13], 0
	s_nop 0
	v_min3_i32 v86, v86, v87, v204
	v_min3_i32 v122, v88, v89, v86
	v_min3_i32 v106, v106, v107, v122
	v_min3_i32 v106, v108, v109, v106
	v_min3_i32 v114, v114, v115, v106
	v_min3_i32 v114, v116, v117, v114
	v_min3_i32 v114, v146, v147, v114
	v_min3_i32 v146, v148, v149, v114
	v_cmp_ge_i32_e32 vcc, v146, v204
	v_mfma_f32_16x16x32_f16 v[50:53], v[50:53], v[6:9], 0
	s_nop 0
	v_cndmask_b32_e32 v147, 3, v205, vcc
	v_mfma_f32_16x16x32_f16 v[46:49], v[46:49], v[6:9], 0
	v_mfma_f32_16x16x32_f16 v[42:45], v[42:45], v[6:9], 0
	s_nop 0
	v_min3_i32 v90, v90, v91, v206
	v_min3_i32 v90, v92, v93, v90
	v_min3_i32 v90, v94, v95, v90
	v_min3_i32 v94, v96, v97, v90
	v_min3_i32 v94, v102, v103, v94
	v_min3_i32 v94, v104, v105, v94
	v_min3_i32 v102, v126, v127, v94
	v_min3_i32 v148, v128, v129, v102
	v_cmp_ge_i32_e32 vcc, v148, v206
	s_waitcnt vmcnt(7)
	v_mfma_f32_16x16x32_f16 v[134:137], v[82:85], v[2:5], 0
	v_cndmask_b32_e32 v149, 3, v207, vcc
	v_mfma_f32_16x16x32_f16 v[138:141], v[82:85], v[34:37], 0
	v_mfma_f32_16x16x32_f16 v[142:145], v[82:85], v[30:33], 0
	v_mfma_f32_16x16x32_f16 v[150:153], v[82:85], v[26:29], 0
	v_mfma_f32_16x16x32_f16 v[154:157], v[82:85], v[22:25], 0
	v_mfma_f32_16x16x32_f16 v[130:133], v[82:85], v[18:21], 0
	v_mfma_f32_16x16x32_f16 v[118:121], v[82:85], v[14:17], 0
	v_mfma_f32_16x16x32_f16 v[98:101], v[82:85], v[10:13], 0
	v_mfma_f32_16x16x32_f16 v[38:41], v[82:85], v[6:9], 0
	s_waitcnt vmcnt(6)
	v_mfma_f32_16x16x32_f16 v[82:85], v[62:65], v[2:5], 0
	s_waitcnt vmcnt(5)
	v_mfma_f32_16x16x32_f16 v[86:89], v[58:61], v[2:5], 0
	s_waitcnt vmcnt(4)
	v_mfma_f32_16x16x32_f16 v[106:109], v[54:57], v[2:5], 0
	s_nop 0
	v_min3_i32 v50, v50, v51, v208
	v_min3_i32 v126, v52, v53, v50
	v_min3_i32 v46, v46, v47, v126
	v_min3_i32 v46, v48, v49, v46
	v_min3_i32 v42, v42, v43, v46
	v_min3_i32 v42, v44, v45, v42
	v_min3_i32 v42, v110, v111, v42
	v_min3_i32 v160, v112, v113, v42
	v_cmp_ge_i32_e32 vcc, v160, v208
	v_mfma_f32_16x16x32_f16 v[114:117], v[62:65], v[34:37], 0
	s_nop 0
	v_cndmask_b32_e32 v161, 3, v209, vcc
	v_mfma_f32_16x16x32_f16 v[122:125], v[58:61], v[34:37], 0
	v_mfma_f32_16x16x32_f16 v[90:93], v[54:57], v[34:37], 0
	s_nop 0
	v_min3_i32 v42, v134, v135, v182
	v_min3_i32 v42, v136, v137, v42
	v_min3_i32 v42, v82, v83, v42
	v_min3_i32 v42, v84, v85, v42
	v_min3_i32 v42, v86, v87, v42
	v_min3_i32 v42, v88, v89, v42
	v_min3_i32 v42, v106, v107, v42
	v_min3_i32 v134, v108, v109, v42
	v_cmp_ge_i32_e32 vcc, v134, v182
	v_mfma_f32_16x16x32_f16 v[94:97], v[62:65], v[30:33], 0
	s_nop 0
	v_cndmask_b32_e32 v135, 4, v183, vcc
	v_mfma_f32_16x16x32_f16 v[102:105], v[58:61], v[30:33], 0
	v_mfma_f32_16x16x32_f16 v[50:53], v[54:57], v[30:33], 0
	v_mfma_f32_16x16x32_f16 v[46:49], v[62:65], v[26:29], 0
	v_mfma_f32_16x16x32_f16 v[110:113], v[62:65], v[22:25], 0
	v_mfma_f32_16x16x32_f16 v[126:129], v[62:65], v[18:21], 0
	v_mfma_f32_16x16x32_f16 v[82:85], v[62:65], v[14:17], 0
	v_mfma_f32_16x16x32_f16 v[86:89], v[62:65], v[10:13], 0
	v_mfma_f32_16x16x32_f16 v[42:45], v[62:65], v[6:9], 0
	v_min3_i32 v62, v138, v139, v174
	v_min3_i32 v106, v140, v141, v62
	v_min3_i32 v106, v114, v115, v106
	v_min3_i32 v106, v116, v117, v106
	v_min3_i32 v114, v122, v123, v106
	v_min3_i32 v114, v124, v125, v114
	v_min3_i32 v90, v90, v91, v114
	v_min3_i32 v122, v92, v93, v90
	v_cmp_ge_i32_e32 vcc, v122, v174
	v_mfma_f32_16x16x32_f16 v[62:65], v[58:61], v[26:29], 0
	s_nop 0
	v_cndmask_b32_e32 v123, 4, v175, vcc
	v_mfma_f32_16x16x32_f16 v[106:109], v[54:57], v[26:29], 0
	s_nop 0
	v_min3_i32 v124, v142, v143, v176
	v_min3_i32 v124, v144, v145, v124
	v_min3_i32 v94, v94, v95, v124
	v_min3_i32 v124, v96, v97, v94
	v_min3_i32 v102, v102, v103, v124
	v_min3_i32 v102, v104, v105, v102
	v_min3_i32 v50, v50, v51, v102
	v_min3_i32 v124, v52, v53, v50
	v_cmp_ge_i32_e32 vcc, v124, v176
	v_mfma_f32_16x16x32_f16 v[90:93], v[58:61], v[22:25], 0
	s_nop 0
	v_cndmask_b32_e32 v125, 4, v177, vcc
	v_mfma_f32_16x16x32_f16 v[114:117], v[54:57], v[22:25], 0
	s_nop 0
	v_min3_i32 v136, v150, v151, v178
	v_min3_i32 v136, v152, v153, v136
	v_min3_i32 v46, v46, v47, v136
	v_min3_i32 v46, v48, v49, v46
	v_min3_i32 v62, v62, v63, v46
	v_min3_i32 v62, v64, v65, v62
	v_min3_i32 v62, v106, v107, v62
	v_min3_i32 v136, v108, v109, v62
	v_cmp_ge_i32_e32 vcc, v136, v178
	v_mfma_f32_16x16x32_f16 v[94:97], v[58:61], v[18:21], 0
	s_nop 0
	v_cndmask_b32_e32 v137, 4, v179, vcc
	v_mfma_f32_16x16x32_f16 v[46:49], v[54:57], v[18:21], 0
	s_nop 0
	v_min3_i32 v138, v154, v155, v166
	v_min3_i32 v138, v156, v157, v138
	v_min3_i32 v110, v110, v111, v138
	v_min3_i32 v110, v112, v113, v110
	v_min3_i32 v90, v90, v91, v110
	v_min3_i32 v90, v92, v93, v90
	v_min3_i32 v110, v114, v115, v90
	v_min3_i32 v138, v116, v117, v110
	v_cmp_ge_i32_e32 vcc, v138, v166
	v_mfma_f32_16x16x32_f16 v[102:105], v[58:61], v[14:17], 0
	v_mov_b32_e32 v154, 0
	v_cndmask_b32_e32 v139, 4, v167, vcc
	v_mfma_f32_16x16x32_f16 v[62:65], v[54:57], v[14:17], 0
	s_nop 0
	v_min3_i32 v114, v130, v131, v158
	v_min3_i32 v130, v132, v133, v114
	v_min3_i32 v126, v126, v127, v130
	v_min3_i32 v126, v128, v129, v126
	v_min3_i32 v94, v94, v95, v126
	v_min3_i32 v94, v96, v97, v94
	v_min3_i32 v46, v46, v47, v94
	v_min3_i32 v126, v48, v49, v46
	v_cmp_ge_i32_e32 vcc, v126, v158
	v_mfma_f32_16x16x32_f16 v[50:53], v[58:61], v[10:13], 0
	s_nop 0
	v_cndmask_b32_e32 v127, 4, v159, vcc
	v_mfma_f32_16x16x32_f16 v[106:109], v[54:57], v[10:13], 0
	s_nop 0
	v_min3_i32 v118, v118, v119, v146
	v_min3_i32 v118, v120, v121, v118
	v_min3_i32 v82, v82, v83, v118
	v_min3_i32 v118, v84, v85, v82
	v_min3_i32 v102, v102, v103, v118
	v_min3_i32 v102, v104, v105, v102
	v_min3_i32 v62, v62, v63, v102
	v_min3_i32 v102, v64, v65, v62
	v_cmp_ge_i32_e32 vcc, v102, v146
	v_mfma_f32_16x16x32_f16 v[58:61], v[58:61], v[6:9], 0
	v_and_b32_e32 v146, 7, v0
	v_cndmask_b32_e32 v103, 4, v147, vcc
	v_mfma_f32_16x16x32_f16 v[54:57], v[54:57], v[6:9], 0
	s_nop 0
	v_min3_i32 v98, v98, v99, v148
	v_min3_i32 v104, v100, v101, v98
	v_min3_i32 v86, v86, v87, v104
	v_min3_i32 v86, v88, v89, v86
	v_min3_i32 v50, v50, v51, v86
	v_min3_i32 v50, v52, v53, v50
	v_min3_i32 v50, v106, v107, v50
	v_min3_i32 v104, v108, v109, v50
	v_cmp_ge_i32_e32 vcc, v104, v148
	s_waitcnt vmcnt(3)
	v_mfma_f32_16x16x32_f16 v[90:93], v[78:81], v[2:5], 0
	v_cndmask_b32_e32 v105, 4, v149, vcc
	s_waitcnt vmcnt(2)
	v_mfma_f32_16x16x32_f16 v[110:113], v[74:77], v[2:5], 0
	s_waitcnt vmcnt(1)
	v_mfma_f32_16x16x32_f16 v[114:117], v[70:73], v[2:5], 0
	s_waitcnt vmcnt(0)
	v_mfma_f32_16x16x32_f16 v[2:5], v[66:69], v[2:5], 0
	s_nop 0
	v_min3_i32 v38, v38, v39, v160
	v_min3_i32 v38, v40, v41, v38
	v_min3_i32 v38, v42, v43, v38
	v_min3_i32 v42, v44, v45, v38
	v_min3_i32 v42, v58, v59, v42
	v_min3_i32 v42, v60, v61, v42
	v_min3_i32 v54, v54, v55, v42
	v_min3_i32 v106, v56, v57, v54
	v_cmp_ge_i32_e32 vcc, v106, v160
	v_mfma_f32_16x16x32_f16 v[46:49], v[78:81], v[34:37], 0
	s_nop 0
	v_cndmask_b32_e32 v107, 4, v161, vcc
	v_mfma_f32_16x16x32_f16 v[94:97], v[74:77], v[34:37], 0
	v_mfma_f32_16x16x32_f16 v[82:85], v[70:73], v[34:37], 0
	v_mfma_f32_16x16x32_f16 v[34:37], v[66:69], v[34:37], 0
	s_nop 0
	v_min3_i32 v54, v90, v91, v134
	v_min3_i32 v58, v92, v93, v54
	v_min3_i32 v58, v110, v111, v58
	v_min3_i32 v58, v112, v113, v58
	v_min3_i32 v90, v114, v115, v58
	v_min3_i32 v90, v116, v117, v90
	v_min3_i32 v2, v2, v3, v90
	v_min3_i32 v91, v4, v5, v2
	v_cmp_ge_i32_e32 vcc, v91, v134
	v_mfma_f32_16x16x32_f16 v[62:65], v[78:81], v[30:33], 0
	s_nop 0
	v_cndmask_b32_e32 v90, 5, v135, vcc
	v_add_u32_e32 v251, s3, v90
	v_lshl_or_b32 v90, v251, 2, v253
	ds_min_u64 v252, v[90:91] offset:16384
	v_mfma_f32_16x16x32_f16 v[98:101], v[74:77], v[30:33], 0
	v_mfma_f32_16x16x32_f16 v[86:89], v[70:73], v[30:33], 0
	v_mfma_f32_16x16x32_f16 v[30:33], v[66:69], v[30:33], 0
	s_nop 0
	v_min3_i32 v46, v46, v47, v122
	v_min3_i32 v46, v48, v49, v46
	v_min3_i32 v46, v94, v95, v46
	v_min3_i32 v92, v96, v97, v46
	v_min3_i32 v82, v82, v83, v92
	v_min3_i32 v82, v84, v85, v82
	v_min3_i32 v34, v34, v35, v82
	v_min3_i32 v93, v36, v37, v34
	v_cmp_ge_i32_e32 vcc, v93, v122
	v_mfma_f32_16x16x32_f16 v[50:53], v[78:81], v[26:29], 0
	s_nop 0
	v_cndmask_b32_e32 v92, 5, v123, vcc
	v_add_u32_e32 v251, s3, v92
	v_lshl_or_b32 v92, v251, 2, v253
	ds_min_u64 v252, v[92:93] offset:16512
	v_mfma_f32_16x16x32_f16 v[38:41], v[74:77], v[26:29], 0
	v_mfma_f32_16x16x32_f16 v[42:45], v[70:73], v[26:29], 0
	v_mfma_f32_16x16x32_f16 v[26:29], v[66:69], v[26:29], 0
	s_nop 0
	v_min3_i32 v62, v62, v63, v124
	v_min3_i32 v62, v64, v65, v62
	v_min3_i32 v62, v98, v99, v62
	v_min3_i32 v62, v100, v101, v62
	v_min3_i32 v86, v86, v87, v62
	v_min3_i32 v86, v88, v89, v86
	v_min3_i32 v30, v30, v31, v86
	v_min3_i32 v95, v32, v33, v30
	v_cmp_ge_i32_e32 vcc, v95, v124
	v_mfma_f32_16x16x32_f16 v[54:57], v[78:81], v[22:25], 0
	s_nop 0
	v_cndmask_b32_e32 v94, 5, v125, vcc
	v_add_u32_e32 v251, s3, v94
	v_lshl_or_b32 v94, v251, 2, v253
	ds_min_u64 v252, v[94:95] offset:16640
	v_mfma_f32_16x16x32_f16 v[58:61], v[74:77], v[22:25], 0
	v_mfma_f32_16x16x32_f16 v[2:5], v[70:73], v[22:25], 0
	v_mfma_f32_16x16x32_f16 v[22:25], v[66:69], v[22:25], 0
	s_nop 0
	v_min3_i32 v50, v50, v51, v136
	v_min3_i32 v50, v52, v53, v50
	v_min3_i32 v38, v38, v39, v50
	v_min3_i32 v38, v40, v41, v38
	v_min3_i32 v38, v42, v43, v38
	v_min3_i32 v38, v44, v45, v38
	v_min3_i32 v26, v26, v27, v38
	v_min3_i32 v51, v28, v29, v26
	v_cmp_ge_i32_e32 vcc, v51, v136
	v_mfma_f32_16x16x32_f16 v[46:49], v[78:81], v[18:21], 0
	s_nop 0
	v_cndmask_b32_e32 v50, 5, v137, vcc
	v_add_u32_e32 v251, s3, v50
	v_lshl_or_b32 v50, v251, 2, v253
	ds_min_u64 v252, v[50:51] offset:16768
	v_mfma_f32_16x16x32_f16 v[82:85], v[74:77], v[18:21], 0
	v_mfma_f32_16x16x32_f16 v[34:37], v[70:73], v[18:21], 0
	v_mfma_f32_16x16x32_f16 v[18:21], v[66:69], v[18:21], 0
	s_nop 0
	v_min3_i32 v42, v54, v55, v138
	v_min3_i32 v52, v56, v57, v42
	v_min3_i32 v52, v58, v59, v52
	v_min3_i32 v52, v60, v61, v52
	v_min3_i32 v2, v2, v3, v52
	v_min3_i32 v2, v4, v5, v2
	v_min3_i32 v2, v22, v23, v2
	v_min3_i32 v53, v24, v25, v2
	v_cmp_ge_i32_e32 vcc, v53, v138
	v_mfma_f32_16x16x32_f16 v[62:65], v[78:81], v[14:17], 0
	s_nop 0
	v_cndmask_b32_e32 v52, 5, v139, vcc
	v_add_u32_e32 v251, s3, v52
	v_lshl_or_b32 v52, v251, 2, v253
	ds_min_u64 v252, v[52:53] offset:16896
	v_mfma_f32_16x16x32_f16 v[30:33], v[74:77], v[14:17], 0
	v_mfma_f32_16x16x32_f16 v[86:89], v[70:73], v[14:17], 0
	v_mfma_f32_16x16x32_f16 v[14:17], v[66:69], v[14:17], 0
	s_nop 0
	v_min3_i32 v46, v46, v47, v126
	v_min3_i32 v46, v48, v49, v46
	v_min3_i32 v54, v82, v83, v46
	v_min3_i32 v54, v84, v85, v54
	v_min3_i32 v34, v34, v35, v54
	v_min3_i32 v34, v36, v37, v34
	v_min3_i32 v18, v18, v19, v34
	v_min3_i32 v19, v20, v21, v18
	v_cmp_ge_i32_e32 vcc, v19, v126
	v_mfma_f32_16x16x32_f16 v[38:41], v[78:81], v[10:13], 0
	s_nop 0
	v_cndmask_b32_e32 v18, 5, v127, vcc
	v_add_u32_e32 v251, s3, v18
	v_lshl_or_b32 v18, v251, 2, v253
	ds_min_u64 v252, v[18:19] offset:17024
	v_mfma_f32_16x16x32_f16 v[26:29], v[74:77], v[10:13], 0
	v_mfma_f32_16x16x32_f16 v[42:45], v[70:73], v[10:13], 0
	v_mfma_f32_16x16x32_f16 v[10:13], v[66:69], v[10:13], 0
	s_nop 0
	v_min3_i32 v20, v62, v63, v102
	v_min3_i32 v20, v64, v65, v20
	v_min3_i32 v20, v30, v31, v20
	v_min3_i32 v20, v32, v33, v20
	v_min3_i32 v20, v86, v87, v20
	v_min3_i32 v20, v88, v89, v20
	v_min3_i32 v14, v14, v15, v20
	v_min3_i32 v15, v16, v17, v14
	v_cmp_ge_i32_e32 vcc, v15, v102
	v_mfma_f32_16x16x32_f16 v[2:5], v[78:81], v[6:9], 0
	v_bfe_u32 v17, v0, 4, 2
	v_cndmask_b32_e32 v14, 5, v103, vcc
	v_add_u32_e32 v251, s3, v14
	v_lshl_or_b32 v14, v251, 2, v253
	ds_min_u64 v252, v[14:15] offset:17152
	v_mfma_f32_16x16x32_f16 v[22:25], v[74:77], v[6:9], 0
	v_mfma_f32_16x16x32_f16 v[46:49], v[70:73], v[6:9], 0
	v_mfma_f32_16x16x32_f16 v[6:9], v[66:69], v[6:9], 0
	s_nop 0
	v_min3_i32 v16, v38, v39, v104
	v_min3_i32 v16, v40, v41, v16
	v_min3_i32 v16, v26, v27, v16
	v_min3_i32 v2, v2, v3, v106
	v_min3_i32 v16, v28, v29, v16
	v_min3_i32 v2, v4, v5, v2
	v_min3_i32 v16, v42, v43, v16
	v_min3_i32 v2, v22, v23, v2
	v_lshlrev_b32_e32 v4, 3, v210
	v_min3_i32 v16, v44, v45, v16
	v_min3_i32 v2, v24, v25, v2
	v_min3_i32 v10, v10, v11, v16
	v_min3_i32 v2, v46, v47, v2
	v_min3_i32 v11, v12, v13, v10
	v_min3_i32 v2, v48, v49, v2
	v_cmp_ge_i32_e32 vcc, v11, v104
	v_min3_i32 v2, v6, v7, v2
	v_cndmask_b32_e32 v10, 5, v105, vcc
	v_add_u32_e32 v251, s3, v10
	v_lshl_or_b32 v10, v251, 2, v253
	ds_min_u64 v252, v[10:11] offset:17280
	v_min3_i32 v3, v8, v9, v2
	v_cmp_ge_i32_e32 vcc, v3, v106
	v_cndmask_b32_e32 v2, 5, v107, vcc
	v_add_u32_e32 v2, s3, v2
	v_bfe_u32 v10, v0, 3, 3
	s_lshl_b32 s3, s15, 3
	v_lshl_or_b32 v2, v2, 2, v17
	v_or_b32_e32 v151, s3, v10
	ds_min_u64 v4, v[2:3] offset:17408
	v_lshlrev_b32_e32 v2, 3, v151
	s_waitcnt lgkmcnt(0)
	s_barrier
	ds_read2st64_b32 v[4:5], v2 offset0:64 offset1:66
	s_add_i32 s2, s3, s11
	s_lshr_b32 s2, s2, 4
	s_add_i32 s2, s2, s8
	s_waitcnt lgkmcnt(0)
	v_ashrrev_i32_e32 v3, 2, v4
	v_mul_hi_i32 v6, v3, s12
	v_lshrrev_b32_e32 v7, 31, v6
	v_add_u32_e32 v6, v6, v7
	v_mul_lo_u32 v7, v6, -6
	v_mul_lo_u32 v6, v6, 24
	v_min_i32_e32 v6, 0xa5, v6
	v_add_lshl_u32 v7, v7, v3, 2
	v_bfe_u32 v3, v0, 2, 1
	v_add3_u32 v152, v6, v3, v7
	v_lshlrev_b32_e32 v6, 2, v4
	v_and_b32_e32 v4, 3, v0
	v_and_or_b32 v153, v6, 12, v4
	v_add_u32_e32 v6, s9, v152
	v_lshl_or_b32 v6, v6, 6, v153
	v_bitop3_b32 v7, s3, 15, v10 bitop3:0xc8
	v_lshl_or_b32 v7, v4, 4, v7
	v_lshl_or_b32 v8, s2, 6, v7
	v_ashrrev_i32_e32 v7, 31, v6
	v_lshl_add_u64 v[6:7], v[6:7], 4, s[6:7]
	v_ashrrev_i32_e32 v9, 31, v8
	v_lshl_add_u64 v[8:9], v[8:9], 4, s[4:5]
	global_load_dwordx4 v[126:129], v[6:7], off
	global_load_dwordx4 v[114:117], v[6:7], off offset:256
	global_load_dwordx4 v[130:133], v[6:7], off offset:2048
	global_load_dwordx4 v[118:121], v[6:7], off offset:2304
	global_load_dwordx4 v[134:137], v[8:9], off
	global_load_dwordx4 v[102:105], v[6:7], off offset:512
	global_load_dwordx4 v[78:81], v[6:7], off offset:768
	global_load_dwordx4 v[106:109], v[6:7], off offset:2560
	global_load_dwordx4 v[82:85], v[6:7], off offset:2816
	v_ashrrev_i32_e32 v6, 2, v5
	v_mul_hi_i32 v7, v6, s12
	v_lshrrev_b32_e32 v11, 31, v7
	v_add_u32_e32 v7, v7, v11
	v_mul_lo_u32 v11, v7, -6
	v_mul_lo_u32 v7, v7, 24
	s_add_i32 s2, s3, 64
	v_min_i32_e32 v7, 0xa5, v7
	v_add_lshl_u32 v6, v11, v6, 2
	s_add_i32 s3, s2, s11
	v_add3_u32 v148, v7, v3, v6
	v_lshlrev_b32_e32 v5, 2, v5
	v_and_or_b32 v149, v5, 12, v4
	v_add_u32_e32 v5, s9, v148
	s_lshr_b32 s3, s3, 4
	v_lshl_or_b32 v6, v5, 6, v149
	s_add_i32 s3, s3, s8
	v_bitop3_b32 v5, s2, 15, v10 bitop3:0xc8
	v_lshl_or_b32 v5, v4, 4, v5
	v_lshl_or_b32 v10, s3, 6, v5
	v_ashrrev_i32_e32 v7, 31, v6
	v_ashrrev_i32_e32 v11, 31, v10
	v_lshl_add_u64 v[6:7], v[6:7], 4, s[6:7]
	v_lshl_add_u64 v[10:11], v[10:11], 4, s[4:5]
	global_load_dwordx4 v[110:113], v[10:11], off
	global_load_dwordx4 v[90:93], v[6:7], off
	global_load_dwordx4 v[62:65], v[6:7], off offset:256
	global_load_dwordx4 v[94:97], v[6:7], off offset:2048
	global_load_dwordx4 v[66:69], v[6:7], off offset:2304
	global_load_dwordx4 v[38:41], v[6:7], off offset:512
	global_load_dwordx4 v[18:21], v[6:7], off offset:768
	global_load_dwordx4 v[42:45], v[6:7], off offset:2560
	global_load_dwordx4 v[22:25], v[6:7], off offset:2816
	s_cmpk_lt_u32 s10, 0x80
	s_cselect_b64 s[2:3], -1, 0
	s_cmpk_gt_u32 s10, 0x7f
	s_cbranch_scc1 .LBB1_4
	v_add_u32_e32 v2, 0x4000, v2
	ds_read_b32 v2, v2 offset:1024
	v_or_b32_e32 v147, 0x80, v151
	v_add_u32_e32 v5, s11, v147
	s_waitcnt lgkmcnt(0)
	v_ashrrev_i32_e32 v6, 2, v2
	v_mul_hi_i32 v7, v6, s12
	v_lshrrev_b32_e32 v8, 31, v7
	v_add_u32_e32 v7, v7, v8
	v_mul_lo_u32 v8, v7, -6
	v_mul_lo_u32 v7, v7, 24
	v_min_i32_e32 v7, 0xa5, v7
	v_add_lshl_u32 v6, v8, v6, 2
	v_add3_u32 v150, v7, v3, v6
	v_lshlrev_b32_e32 v2, 2, v2
	v_lshrrev_b32_e32 v3, 4, v5
	v_and_or_b32 v155, v2, 12, v4
	v_add_u32_e32 v2, s9, v150
	v_add_u32_e32 v3, s8, v3
	v_lshl_or_b32 v2, v2, 6, v155
	v_lshl_or_b32 v4, v4, 4, v151
	v_lshl_or_b32 v4, v3, 6, v4
	v_ashrrev_i32_e32 v3, 31, v2
	v_ashrrev_i32_e32 v5, 31, v4
	v_lshl_add_u64 v[2:3], v[2:3], 4, s[6:7]
	v_lshl_add_u64 v[50:51], v[4:5], 4, s[4:5]
	global_load_dwordx4 v[58:61], v[2:3], off
	global_load_dwordx4 v[46:49], v[2:3], off offset:256
	global_load_dwordx4 v[34:37], v[2:3], off offset:2048
	global_load_dwordx4 v[10:13], v[2:3], off offset:2304
	global_load_dwordx4 v[98:101], v[50:51], off
	global_load_dwordx4 v[30:33], v[2:3], off offset:512
	global_load_dwordx4 v[14:17], v[2:3], off offset:768
	global_load_dwordx4 v[6:9], v[2:3], off offset:2560
	s_nop 0
	global_load_dwordx4 v[2:5], v[2:3], off offset:2816
	s_nop 0
	s_nop 0
	v_lshl_or_b32 v150, v150, 4, v155
	s_branch .LBB1_5
